# speedup vs baseline: 1.0175x; 1.0175x over previous
_Z11prep_kernelPKfS0_S0_PDF16_PfPiS0_S1_:
	s_cmpk_lt_u32 s2, 0xc1
	s_mov_b64 s[4:5], -1
	s_cbranch_scc0 .LBB0_51
	s_cmpk_lg_i32 s2, 0xc0
	s_cbranch_scc0 .LBB0_11
	s_cmp_gt_u32 s2, 63
	s_cbranch_scc0 .LBB0_8
	s_load_dwordx4 s[4:7], s[0:1], 0x0
	s_load_dwordx2 s[28:29], s[0:1], 0x20
	s_sub_u32 s3, s2, 64
	v_readfirstlane_b32 s23, v0
	v_and_b32_e32 v1, 63, v0
	v_lshlrev_b32_e32 v100, 4, v1
	s_lshr_b32 s23, s23, 6
	s_lshr_b32 s27, s3, 1
	s_and_b32 s30, s3, 1
	s_lshl_b32 s8, s27, 12
	s_lshl_b32 s9, s23, 6
	s_add_u32 s8, s8, s9
	s_lshl_b32 s10, s23, 15
	s_lshl_b32 s9, s30, 10
	s_add_u32 s10, s10, s9
	s_waitcnt lgkmcnt(0)
	s_add_u32 s20, s4, s8
	s_addc_u32 s21, s5, 0
	s_add_u32 s24, s6, s10
	s_addc_u32 s25, s7, 0
	global_load_dwordx4 v[34:37], v100, s[24:25]
	global_load_dwordx4 v[38:41], v100, s[24:25] offset:2048
	s_add_u32 s24, s24, 0x1000
	s_addc_u32 s25, s25, 0
	s_load_dwordx8 s[32:39], s[20:21], 0x0
	s_load_dwordx8 s[40:47], s[20:21], 0x200
	s_load_dwordx8 s[48:55], s[20:21], 0x400
	s_load_dwordx8 s[56:63], s[20:21], 0x600
	s_load_dwordx8 s[64:71], s[20:21], 0x800
	s_load_dwordx8 s[72:79], s[20:21], 0xa00
	s_load_dwordx8 s[80:87], s[20:21], 0xc00
	s_load_dwordx8 s[88:95], s[20:21], 0xe00
	global_load_dwordx4 v[42:45], v100, s[24:25]
	global_load_dwordx4 v[46:49], v100, s[24:25] offset:2048
	s_add_u32 s24, s24, 0x1000
	s_addc_u32 s25, s25, 0
	global_load_dwordx4 v[50:53], v100, s[24:25]
	global_load_dwordx4 v[54:57], v100, s[24:25] offset:2048
	s_add_u32 s24, s24, 0x1000
	s_addc_u32 s25, s25, 0
	global_load_dwordx4 v[58:61], v100, s[24:25]
	global_load_dwordx4 v[62:65], v100, s[24:25] offset:2048
	s_add_u32 s24, s24, 0x1000
	s_addc_u32 s25, s25, 0
	global_load_dwordx4 v[66:69], v100, s[24:25]
	global_load_dwordx4 v[70:73], v100, s[24:25] offset:2048
	s_add_u32 s24, s24, 0x1000
	s_addc_u32 s25, s25, 0
	global_load_dwordx4 v[74:77], v100, s[24:25]
	global_load_dwordx4 v[78:81], v100, s[24:25] offset:2048
	s_add_u32 s24, s24, 0x1000
	s_addc_u32 s25, s25, 0
	global_load_dwordx4 v[82:85], v100, s[24:25]
	global_load_dwordx4 v[86:89], v100, s[24:25] offset:2048
	s_add_u32 s24, s24, 0x1000
	s_addc_u32 s25, s25, 0
	global_load_dwordx4 v[90:93], v100, s[24:25]
	global_load_dwordx4 v[94:97], v100, s[24:25] offset:2048
	v_mov_b64_e32 v[2:3], 0
	v_mov_b64_e32 v[4:5], 0
	v_mov_b64_e32 v[6:7], 0
	v_mov_b64_e32 v[8:9], 0
	v_mov_b64_e32 v[10:11], 0
	v_mov_b64_e32 v[12:13], 0
	v_mov_b64_e32 v[14:15], 0
	v_mov_b64_e32 v[16:17], 0
	v_mov_b64_e32 v[18:19], 0
	v_mov_b64_e32 v[20:21], 0
	v_mov_b64_e32 v[22:23], 0
	v_mov_b64_e32 v[24:25], 0
	v_mov_b64_e32 v[26:27], 0
	v_mov_b64_e32 v[28:29], 0
	v_mov_b64_e32 v[30:31], 0
	v_mov_b64_e32 v[32:33], 0
	s_waitcnt lgkmcnt(0)
	s_waitcnt vmcnt(15)
	v_fmac_f32_e32 v2, s32, v34
	v_fmac_f32_e32 v3, s32, v35
	v_fmac_f32_e32 v4, s32, v36
	v_fmac_f32_e32 v5, s32, v37
	v_fmac_f32_e32 v6, s40, v34
	v_fmac_f32_e32 v7, s40, v35
	v_fmac_f32_e32 v8, s40, v36
	v_fmac_f32_e32 v9, s40, v37
	v_fmac_f32_e32 v10, s48, v34
	v_fmac_f32_e32 v11, s48, v35
	v_fmac_f32_e32 v12, s48, v36
	v_fmac_f32_e32 v13, s48, v37
	v_fmac_f32_e32 v14, s56, v34
	v_fmac_f32_e32 v15, s56, v35
	v_fmac_f32_e32 v16, s56, v36
	v_fmac_f32_e32 v17, s56, v37
	v_fmac_f32_e32 v18, s64, v34
	v_fmac_f32_e32 v19, s64, v35
	v_fmac_f32_e32 v20, s64, v36
	v_fmac_f32_e32 v21, s64, v37
	v_fmac_f32_e32 v22, s72, v34
	v_fmac_f32_e32 v23, s72, v35
	v_fmac_f32_e32 v24, s72, v36
	v_fmac_f32_e32 v25, s72, v37
	v_fmac_f32_e32 v26, s80, v34
	v_fmac_f32_e32 v27, s80, v35
	v_fmac_f32_e32 v28, s80, v36
	v_fmac_f32_e32 v29, s80, v37
	v_fmac_f32_e32 v30, s88, v34
	v_fmac_f32_e32 v31, s88, v35
	v_fmac_f32_e32 v32, s88, v36
	v_fmac_f32_e32 v33, s88, v37
	s_waitcnt vmcnt(14)
	v_fmac_f32_e32 v2, s33, v38
	v_fmac_f32_e32 v3, s33, v39
	v_fmac_f32_e32 v4, s33, v40
	v_fmac_f32_e32 v5, s33, v41
	v_fmac_f32_e32 v6, s41, v38
	v_fmac_f32_e32 v7, s41, v39
	v_fmac_f32_e32 v8, s41, v40
	v_fmac_f32_e32 v9, s41, v41
	v_fmac_f32_e32 v10, s49, v38
	v_fmac_f32_e32 v11, s49, v39
	v_fmac_f32_e32 v12, s49, v40
	v_fmac_f32_e32 v13, s49, v41
	v_fmac_f32_e32 v14, s57, v38
	v_fmac_f32_e32 v15, s57, v39
	v_fmac_f32_e32 v16, s57, v40
	v_fmac_f32_e32 v17, s57, v41
	v_fmac_f32_e32 v18, s65, v38
	v_fmac_f32_e32 v19, s65, v39
	v_fmac_f32_e32 v20, s65, v40
	v_fmac_f32_e32 v21, s65, v41
	v_fmac_f32_e32 v22, s73, v38
	v_fmac_f32_e32 v23, s73, v39
	v_fmac_f32_e32 v24, s73, v40
	v_fmac_f32_e32 v25, s73, v41
	v_fmac_f32_e32 v26, s81, v38
	v_fmac_f32_e32 v27, s81, v39
	v_fmac_f32_e32 v28, s81, v40
	v_fmac_f32_e32 v29, s81, v41
	v_fmac_f32_e32 v30, s89, v38
	v_fmac_f32_e32 v31, s89, v39
	v_fmac_f32_e32 v32, s89, v40
	v_fmac_f32_e32 v33, s89, v41
	s_waitcnt vmcnt(13)
	v_fmac_f32_e32 v2, s34, v42
	v_fmac_f32_e32 v3, s34, v43
	v_fmac_f32_e32 v4, s34, v44
	v_fmac_f32_e32 v5, s34, v45
	v_fmac_f32_e32 v6, s42, v42
	v_fmac_f32_e32 v7, s42, v43
	v_fmac_f32_e32 v8, s42, v44
	v_fmac_f32_e32 v9, s42, v45
	v_fmac_f32_e32 v10, s50, v42
	v_fmac_f32_e32 v11, s50, v43
	v_fmac_f32_e32 v12, s50, v44
	v_fmac_f32_e32 v13, s50, v45
	v_fmac_f32_e32 v14, s58, v42
	v_fmac_f32_e32 v15, s58, v43
	v_fmac_f32_e32 v16, s58, v44
	v_fmac_f32_e32 v17, s58, v45
	v_fmac_f32_e32 v18, s66, v42
	v_fmac_f32_e32 v19, s66, v43
	v_fmac_f32_e32 v20, s66, v44
	v_fmac_f32_e32 v21, s66, v45
	v_fmac_f32_e32 v22, s74, v42
	v_fmac_f32_e32 v23, s74, v43
	v_fmac_f32_e32 v24, s74, v44
	v_fmac_f32_e32 v25, s74, v45
	v_fmac_f32_e32 v26, s82, v42
	v_fmac_f32_e32 v27, s82, v43
	v_fmac_f32_e32 v28, s82, v44
	v_fmac_f32_e32 v29, s82, v45
	v_fmac_f32_e32 v30, s90, v42
	v_fmac_f32_e32 v31, s90, v43
	v_fmac_f32_e32 v32, s90, v44
	v_fmac_f32_e32 v33, s90, v45
	s_waitcnt vmcnt(12)
	v_fmac_f32_e32 v2, s35, v46
	v_fmac_f32_e32 v3, s35, v47
	v_fmac_f32_e32 v4, s35, v48
	v_fmac_f32_e32 v5, s35, v49
	v_fmac_f32_e32 v6, s43, v46
	v_fmac_f32_e32 v7, s43, v47
	v_fmac_f32_e32 v8, s43, v48
	v_fmac_f32_e32 v9, s43, v49
	v_fmac_f32_e32 v10, s51, v46
	v_fmac_f32_e32 v11, s51, v47
	v_fmac_f32_e32 v12, s51, v48
	v_fmac_f32_e32 v13, s51, v49
	v_fmac_f32_e32 v14, s59, v46
	v_fmac_f32_e32 v15, s59, v47
	v_fmac_f32_e32 v16, s59, v48
	v_fmac_f32_e32 v17, s59, v49
	v_fmac_f32_e32 v18, s67, v46
	v_fmac_f32_e32 v19, s67, v47
	v_fmac_f32_e32 v20, s67, v48
	v_fmac_f32_e32 v21, s67, v49
	v_fmac_f32_e32 v22, s75, v46
	v_fmac_f32_e32 v23, s75, v47
	v_fmac_f32_e32 v24, s75, v48
	v_fmac_f32_e32 v25, s75, v49
	v_fmac_f32_e32 v26, s83, v46
	v_fmac_f32_e32 v27, s83, v47
	v_fmac_f32_e32 v28, s83, v48
	v_fmac_f32_e32 v29, s83, v49
	v_fmac_f32_e32 v30, s91, v46
	v_fmac_f32_e32 v31, s91, v47
	v_fmac_f32_e32 v32, s91, v48
	v_fmac_f32_e32 v33, s91, v49
	s_waitcnt vmcnt(11)
	v_fmac_f32_e32 v2, s36, v50
	v_fmac_f32_e32 v3, s36, v51
	v_fmac_f32_e32 v4, s36, v52
	v_fmac_f32_e32 v5, s36, v53
	v_fmac_f32_e32 v6, s44, v50
	v_fmac_f32_e32 v7, s44, v51
	v_fmac_f32_e32 v8, s44, v52
	v_fmac_f32_e32 v9, s44, v53
	v_fmac_f32_e32 v10, s52, v50
	v_fmac_f32_e32 v11, s52, v51
	v_fmac_f32_e32 v12, s52, v52
	v_fmac_f32_e32 v13, s52, v53
	v_fmac_f32_e32 v14, s60, v50
	v_fmac_f32_e32 v15, s60, v51
	v_fmac_f32_e32 v16, s60, v52
	v_fmac_f32_e32 v17, s60, v53
	v_fmac_f32_e32 v18, s68, v50
	v_fmac_f32_e32 v19, s68, v51
	v_fmac_f32_e32 v20, s68, v52
	v_fmac_f32_e32 v21, s68, v53
	v_fmac_f32_e32 v22, s76, v50
	v_fmac_f32_e32 v23, s76, v51
	v_fmac_f32_e32 v24, s76, v52
	v_fmac_f32_e32 v25, s76, v53
	v_fmac_f32_e32 v26, s84, v50
	v_fmac_f32_e32 v27, s84, v51
	v_fmac_f32_e32 v28, s84, v52
	v_fmac_f32_e32 v29, s84, v53
	v_fmac_f32_e32 v30, s92, v50
	v_fmac_f32_e32 v31, s92, v51
	v_fmac_f32_e32 v32, s92, v52
	v_fmac_f32_e32 v33, s92, v53
	s_waitcnt vmcnt(10)
	v_fmac_f32_e32 v2, s37, v54
	v_fmac_f32_e32 v3, s37, v55
	v_fmac_f32_e32 v4, s37, v56
	v_fmac_f32_e32 v5, s37, v57
	v_fmac_f32_e32 v6, s45, v54
	v_fmac_f32_e32 v7, s45, v55
	v_fmac_f32_e32 v8, s45, v56
	v_fmac_f32_e32 v9, s45, v57
	v_fmac_f32_e32 v10, s53, v54
	v_fmac_f32_e32 v11, s53, v55
	v_fmac_f32_e32 v12, s53, v56
	v_fmac_f32_e32 v13, s53, v57
	v_fmac_f32_e32 v14, s61, v54
	v_fmac_f32_e32 v15, s61, v55
	v_fmac_f32_e32 v16, s61, v56
	v_fmac_f32_e32 v17, s61, v57
	v_fmac_f32_e32 v18, s69, v54
	v_fmac_f32_e32 v19, s69, v55
	v_fmac_f32_e32 v20, s69, v56
	v_fmac_f32_e32 v21, s69, v57
	v_fmac_f32_e32 v22, s77, v54
	v_fmac_f32_e32 v23, s77, v55
	v_fmac_f32_e32 v24, s77, v56
	v_fmac_f32_e32 v25, s77, v57
	v_fmac_f32_e32 v26, s85, v54
	v_fmac_f32_e32 v27, s85, v55
	v_fmac_f32_e32 v28, s85, v56
	v_fmac_f32_e32 v29, s85, v57
	v_fmac_f32_e32 v30, s93, v54
	v_fmac_f32_e32 v31, s93, v55
	v_fmac_f32_e32 v32, s93, v56
	v_fmac_f32_e32 v33, s93, v57
	s_waitcnt vmcnt(9)
	v_fmac_f32_e32 v2, s38, v58
	v_fmac_f32_e32 v3, s38, v59
	v_fmac_f32_e32 v4, s38, v60
	v_fmac_f32_e32 v5, s38, v61
	v_fmac_f32_e32 v6, s46, v58
	v_fmac_f32_e32 v7, s46, v59
	v_fmac_f32_e32 v8, s46, v60
	v_fmac_f32_e32 v9, s46, v61
	v_fmac_f32_e32 v10, s54, v58
	v_fmac_f32_e32 v11, s54, v59
	v_fmac_f32_e32 v12, s54, v60
	v_fmac_f32_e32 v13, s54, v61
	v_fmac_f32_e32 v14, s62, v58
	v_fmac_f32_e32 v15, s62, v59
	v_fmac_f32_e32 v16, s62, v60
	v_fmac_f32_e32 v17, s62, v61
	v_fmac_f32_e32 v18, s70, v58
	v_fmac_f32_e32 v19, s70, v59
	v_fmac_f32_e32 v20, s70, v60
	v_fmac_f32_e32 v21, s70, v61
	v_fmac_f32_e32 v22, s78, v58
	v_fmac_f32_e32 v23, s78, v59
	v_fmac_f32_e32 v24, s78, v60
	v_fmac_f32_e32 v25, s78, v61
	v_fmac_f32_e32 v26, s86, v58
	v_fmac_f32_e32 v27, s86, v59
	v_fmac_f32_e32 v28, s86, v60
	v_fmac_f32_e32 v29, s86, v61
	v_fmac_f32_e32 v30, s94, v58
	v_fmac_f32_e32 v31, s94, v59
	v_fmac_f32_e32 v32, s94, v60
	v_fmac_f32_e32 v33, s94, v61
	s_waitcnt vmcnt(8)
	v_fmac_f32_e32 v2, s39, v62
	v_fmac_f32_e32 v3, s39, v63
	v_fmac_f32_e32 v4, s39, v64
	v_fmac_f32_e32 v5, s39, v65
	v_fmac_f32_e32 v6, s47, v62
	v_fmac_f32_e32 v7, s47, v63
	v_fmac_f32_e32 v8, s47, v64
	v_fmac_f32_e32 v9, s47, v65
	v_fmac_f32_e32 v10, s55, v62
	v_fmac_f32_e32 v11, s55, v63
	v_fmac_f32_e32 v12, s55, v64
	v_fmac_f32_e32 v13, s55, v65
	v_fmac_f32_e32 v14, s63, v62
	v_fmac_f32_e32 v15, s63, v63
	v_fmac_f32_e32 v16, s63, v64
	v_fmac_f32_e32 v17, s63, v65
	v_fmac_f32_e32 v18, s71, v62
	v_fmac_f32_e32 v19, s71, v63
	v_fmac_f32_e32 v20, s71, v64
	v_fmac_f32_e32 v21, s71, v65
	v_fmac_f32_e32 v22, s79, v62
	v_fmac_f32_e32 v23, s79, v63
	v_fmac_f32_e32 v24, s79, v64
	v_fmac_f32_e32 v25, s79, v65
	v_fmac_f32_e32 v26, s87, v62
	v_fmac_f32_e32 v27, s87, v63
	v_fmac_f32_e32 v28, s87, v64
	v_fmac_f32_e32 v29, s87, v65
	v_fmac_f32_e32 v30, s95, v62
	v_fmac_f32_e32 v31, s95, v63
	v_fmac_f32_e32 v32, s95, v64
	v_fmac_f32_e32 v33, s95, v65
	s_nop 0
	s_load_dwordx8 s[32:39], s[20:21], 0x20
	s_load_dwordx8 s[40:47], s[20:21], 0x220
	s_load_dwordx8 s[48:55], s[20:21], 0x420
	s_load_dwordx8 s[56:63], s[20:21], 0x620
	s_load_dwordx8 s[64:71], s[20:21], 0x820
	s_load_dwordx8 s[72:79], s[20:21], 0xa20
	s_load_dwordx8 s[80:87], s[20:21], 0xc20
	s_load_dwordx8 s[88:95], s[20:21], 0xe20
	s_waitcnt lgkmcnt(0)
	s_waitcnt vmcnt(7)
	v_fmac_f32_e32 v2, s32, v66
	v_fmac_f32_e32 v3, s32, v67
	v_fmac_f32_e32 v4, s32, v68
	v_fmac_f32_e32 v5, s32, v69
	v_fmac_f32_e32 v6, s40, v66
	v_fmac_f32_e32 v7, s40, v67
	v_fmac_f32_e32 v8, s40, v68
	v_fmac_f32_e32 v9, s40, v69
	v_fmac_f32_e32 v10, s48, v66
	v_fmac_f32_e32 v11, s48, v67
	v_fmac_f32_e32 v12, s48, v68
	v_fmac_f32_e32 v13, s48, v69
	v_fmac_f32_e32 v14, s56, v66
	v_fmac_f32_e32 v15, s56, v67
	v_fmac_f32_e32 v16, s56, v68
	v_fmac_f32_e32 v17, s56, v69
	v_fmac_f32_e32 v18, s64, v66
	v_fmac_f32_e32 v19, s64, v67
	v_fmac_f32_e32 v20, s64, v68
	v_fmac_f32_e32 v21, s64, v69
	v_fmac_f32_e32 v22, s72, v66
	v_fmac_f32_e32 v23, s72, v67
	v_fmac_f32_e32 v24, s72, v68
	v_fmac_f32_e32 v25, s72, v69
	v_fmac_f32_e32 v26, s80, v66
	v_fmac_f32_e32 v27, s80, v67
	v_fmac_f32_e32 v28, s80, v68
	v_fmac_f32_e32 v29, s80, v69
	v_fmac_f32_e32 v30, s88, v66
	v_fmac_f32_e32 v31, s88, v67
	v_fmac_f32_e32 v32, s88, v68
	v_fmac_f32_e32 v33, s88, v69
	s_waitcnt vmcnt(6)
	v_fmac_f32_e32 v2, s33, v70
	v_fmac_f32_e32 v3, s33, v71
	v_fmac_f32_e32 v4, s33, v72
	v_fmac_f32_e32 v5, s33, v73
	v_fmac_f32_e32 v6, s41, v70
	v_fmac_f32_e32 v7, s41, v71
	v_fmac_f32_e32 v8, s41, v72
	v_fmac_f32_e32 v9, s41, v73
	v_fmac_f32_e32 v10, s49, v70
	v_fmac_f32_e32 v11, s49, v71
	v_fmac_f32_e32 v12, s49, v72
	v_fmac_f32_e32 v13, s49, v73
	v_fmac_f32_e32 v14, s57, v70
	v_fmac_f32_e32 v15, s57, v71
	v_fmac_f32_e32 v16, s57, v72
	v_fmac_f32_e32 v17, s57, v73
	v_fmac_f32_e32 v18, s65, v70
	v_fmac_f32_e32 v19, s65, v71
	v_fmac_f32_e32 v20, s65, v72
	v_fmac_f32_e32 v21, s65, v73
	v_fmac_f32_e32 v22, s73, v70
	v_fmac_f32_e32 v23, s73, v71
	v_fmac_f32_e32 v24, s73, v72
	v_fmac_f32_e32 v25, s73, v73
	v_fmac_f32_e32 v26, s81, v70
	v_fmac_f32_e32 v27, s81, v71
	v_fmac_f32_e32 v28, s81, v72
	v_fmac_f32_e32 v29, s81, v73
	v_fmac_f32_e32 v30, s89, v70
	v_fmac_f32_e32 v31, s89, v71
	v_fmac_f32_e32 v32, s89, v72
	v_fmac_f32_e32 v33, s89, v73
	s_waitcnt vmcnt(5)
	v_fmac_f32_e32 v2, s34, v74
	v_fmac_f32_e32 v3, s34, v75
	v_fmac_f32_e32 v4, s34, v76
	v_fmac_f32_e32 v5, s34, v77
	v_fmac_f32_e32 v6, s42, v74
	v_fmac_f32_e32 v7, s42, v75
	v_fmac_f32_e32 v8, s42, v76
	v_fmac_f32_e32 v9, s42, v77
	v_fmac_f32_e32 v10, s50, v74
	v_fmac_f32_e32 v11, s50, v75
	v_fmac_f32_e32 v12, s50, v76
	v_fmac_f32_e32 v13, s50, v77
	v_fmac_f32_e32 v14, s58, v74
	v_fmac_f32_e32 v15, s58, v75
	v_fmac_f32_e32 v16, s58, v76
	v_fmac_f32_e32 v17, s58, v77
	v_fmac_f32_e32 v18, s66, v74
	v_fmac_f32_e32 v19, s66, v75
	v_fmac_f32_e32 v20, s66, v76
	v_fmac_f32_e32 v21, s66, v77
	v_fmac_f32_e32 v22, s74, v74
	v_fmac_f32_e32 v23, s74, v75
	v_fmac_f32_e32 v24, s74, v76
	v_fmac_f32_e32 v25, s74, v77
	v_fmac_f32_e32 v26, s82, v74
	v_fmac_f32_e32 v27, s82, v75
	v_fmac_f32_e32 v28, s82, v76
	v_fmac_f32_e32 v29, s82, v77
	v_fmac_f32_e32 v30, s90, v74
	v_fmac_f32_e32 v31, s90, v75
	v_fmac_f32_e32 v32, s90, v76
	v_fmac_f32_e32 v33, s90, v77
	s_waitcnt vmcnt(4)
	v_fmac_f32_e32 v2, s35, v78
	v_fmac_f32_e32 v3, s35, v79
	v_fmac_f32_e32 v4, s35, v80
	v_fmac_f32_e32 v5, s35, v81
	v_fmac_f32_e32 v6, s43, v78
	v_fmac_f32_e32 v7, s43, v79
	v_fmac_f32_e32 v8, s43, v80
	v_fmac_f32_e32 v9, s43, v81
	v_fmac_f32_e32 v10, s51, v78
	v_fmac_f32_e32 v11, s51, v79
	v_fmac_f32_e32 v12, s51, v80
	v_fmac_f32_e32 v13, s51, v81
	v_fmac_f32_e32 v14, s59, v78
	v_fmac_f32_e32 v15, s59, v79
	v_fmac_f32_e32 v16, s59, v80
	v_fmac_f32_e32 v17, s59, v81
	v_fmac_f32_e32 v18, s67, v78
	v_fmac_f32_e32 v19, s67, v79
	v_fmac_f32_e32 v20, s67, v80
	v_fmac_f32_e32 v21, s67, v81
	v_fmac_f32_e32 v22, s75, v78
	v_fmac_f32_e32 v23, s75, v79
	v_fmac_f32_e32 v24, s75, v80
	v_fmac_f32_e32 v25, s75, v81
	v_fmac_f32_e32 v26, s83, v78
	v_fmac_f32_e32 v27, s83, v79
	v_fmac_f32_e32 v28, s83, v80
	v_fmac_f32_e32 v29, s83, v81
	v_fmac_f32_e32 v30, s91, v78
	v_fmac_f32_e32 v31, s91, v79
	v_fmac_f32_e32 v32, s91, v80
	v_fmac_f32_e32 v33, s91, v81
	s_waitcnt vmcnt(3)
	v_fmac_f32_e32 v2, s36, v82
	v_fmac_f32_e32 v3, s36, v83
	v_fmac_f32_e32 v4, s36, v84
	v_fmac_f32_e32 v5, s36, v85
	v_fmac_f32_e32 v6, s44, v82
	v_fmac_f32_e32 v7, s44, v83
	v_fmac_f32_e32 v8, s44, v84
	v_fmac_f32_e32 v9, s44, v85
	v_fmac_f32_e32 v10, s52, v82
	v_fmac_f32_e32 v11, s52, v83
	v_fmac_f32_e32 v12, s52, v84
	v_fmac_f32_e32 v13, s52, v85
	v_fmac_f32_e32 v14, s60, v82
	v_fmac_f32_e32 v15, s60, v83
	v_fmac_f32_e32 v16, s60, v84
	v_fmac_f32_e32 v17, s60, v85
	v_fmac_f32_e32 v18, s68, v82
	v_fmac_f32_e32 v19, s68, v83
	v_fmac_f32_e32 v20, s68, v84
	v_fmac_f32_e32 v21, s68, v85
	v_fmac_f32_e32 v22, s76, v82
	v_fmac_f32_e32 v23, s76, v83
	v_fmac_f32_e32 v24, s76, v84
	v_fmac_f32_e32 v25, s76, v85
	v_fmac_f32_e32 v26, s84, v82
	v_fmac_f32_e32 v27, s84, v83
	v_fmac_f32_e32 v28, s84, v84
	v_fmac_f32_e32 v29, s84, v85
	v_fmac_f32_e32 v30, s92, v82
	v_fmac_f32_e32 v31, s92, v83
	v_fmac_f32_e32 v32, s92, v84
	v_fmac_f32_e32 v33, s92, v85
	s_waitcnt vmcnt(2)
	v_fmac_f32_e32 v2, s37, v86
	v_fmac_f32_e32 v3, s37, v87
	v_fmac_f32_e32 v4, s37, v88
	v_fmac_f32_e32 v5, s37, v89
	v_fmac_f32_e32 v6, s45, v86
	v_fmac_f32_e32 v7, s45, v87
	v_fmac_f32_e32 v8, s45, v88
	v_fmac_f32_e32 v9, s45, v89
	v_fmac_f32_e32 v10, s53, v86
	v_fmac_f32_e32 v11, s53, v87
	v_fmac_f32_e32 v12, s53, v88
	v_fmac_f32_e32 v13, s53, v89
	v_fmac_f32_e32 v14, s61, v86
	v_fmac_f32_e32 v15, s61, v87
	v_fmac_f32_e32 v16, s61, v88
	v_fmac_f32_e32 v17, s61, v89
	v_fmac_f32_e32 v18, s69, v86
	v_fmac_f32_e32 v19, s69, v87
	v_fmac_f32_e32 v20, s69, v88
	v_fmac_f32_e32 v21, s69, v89
	v_fmac_f32_e32 v22, s77, v86
	v_fmac_f32_e32 v23, s77, v87
	v_fmac_f32_e32 v24, s77, v88
	v_fmac_f32_e32 v25, s77, v89
	v_fmac_f32_e32 v26, s85, v86
	v_fmac_f32_e32 v27, s85, v87
	v_fmac_f32_e32 v28, s85, v88
	v_fmac_f32_e32 v29, s85, v89
	v_fmac_f32_e32 v30, s93, v86
	v_fmac_f32_e32 v31, s93, v87
	v_fmac_f32_e32 v32, s93, v88
	v_fmac_f32_e32 v33, s93, v89
	s_waitcnt vmcnt(1)
	v_fmac_f32_e32 v2, s38, v90
	v_fmac_f32_e32 v3, s38, v91
	v_fmac_f32_e32 v4, s38, v92
	v_fmac_f32_e32 v5, s38, v93
	v_fmac_f32_e32 v6, s46, v90
	v_fmac_f32_e32 v7, s46, v91
	v_fmac_f32_e32 v8, s46, v92
	v_fmac_f32_e32 v9, s46, v93
	v_fmac_f32_e32 v10, s54, v90
	v_fmac_f32_e32 v11, s54, v91
	v_fmac_f32_e32 v12, s54, v92
	v_fmac_f32_e32 v13, s54, v93
	v_fmac_f32_e32 v14, s62, v90
	v_fmac_f32_e32 v15, s62, v91
	v_fmac_f32_e32 v16, s62, v92
	v_fmac_f32_e32 v17, s62, v93
	v_fmac_f32_e32 v18, s70, v90
	v_fmac_f32_e32 v19, s70, v91
	v_fmac_f32_e32 v20, s70, v92
	v_fmac_f32_e32 v21, s70, v93
	v_fmac_f32_e32 v22, s78, v90
	v_fmac_f32_e32 v23, s78, v91
	v_fmac_f32_e32 v24, s78, v92
	v_fmac_f32_e32 v25, s78, v93
	v_fmac_f32_e32 v26, s86, v90
	v_fmac_f32_e32 v27, s86, v91
	v_fmac_f32_e32 v28, s86, v92
	v_fmac_f32_e32 v29, s86, v93
	v_fmac_f32_e32 v30, s94, v90
	v_fmac_f32_e32 v31, s94, v91
	v_fmac_f32_e32 v32, s94, v92
	v_fmac_f32_e32 v33, s94, v93
	s_waitcnt vmcnt(0)
	v_fmac_f32_e32 v2, s39, v94
	v_fmac_f32_e32 v3, s39, v95
	v_fmac_f32_e32 v4, s39, v96
	v_fmac_f32_e32 v5, s39, v97
	v_fmac_f32_e32 v6, s47, v94
	v_fmac_f32_e32 v7, s47, v95
	v_fmac_f32_e32 v8, s47, v96
	v_fmac_f32_e32 v9, s47, v97
	v_fmac_f32_e32 v10, s55, v94
	v_fmac_f32_e32 v11, s55, v95
	v_fmac_f32_e32 v12, s55, v96
	v_fmac_f32_e32 v13, s55, v97
	v_fmac_f32_e32 v14, s63, v94
	v_fmac_f32_e32 v15, s63, v95
	v_fmac_f32_e32 v16, s63, v96
	v_fmac_f32_e32 v17, s63, v97
	v_fmac_f32_e32 v18, s71, v94
	v_fmac_f32_e32 v19, s71, v95
	v_fmac_f32_e32 v20, s71, v96
	v_fmac_f32_e32 v21, s71, v97
	v_fmac_f32_e32 v22, s79, v94
	v_fmac_f32_e32 v23, s79, v95
	v_fmac_f32_e32 v24, s79, v96
	v_fmac_f32_e32 v25, s79, v97
	v_fmac_f32_e32 v26, s87, v94
	v_fmac_f32_e32 v27, s87, v95
	v_fmac_f32_e32 v28, s87, v96
	v_fmac_f32_e32 v29, s87, v97
	v_fmac_f32_e32 v30, s95, v94
	v_fmac_f32_e32 v31, s95, v95
	v_fmac_f32_e32 v32, s95, v96
	v_fmac_f32_e32 v33, s95, v97
	s_lshl_b32 s9, s23, 13
	v_add_u32_e32 v98, s9, v100
	ds_write_b128 v98, v[2:5] offset:0
	ds_write_b128 v98, v[6:9] offset:1024
	ds_write_b128 v98, v[10:13] offset:2048
	ds_write_b128 v98, v[14:17] offset:3072
	ds_write_b128 v98, v[18:21] offset:4096
	ds_write_b128 v98, v[22:25] offset:5120
	ds_write_b128 v98, v[26:29] offset:6144
	ds_write_b128 v98, v[30:33] offset:7168
	s_lshl_b32 s9, s23, 10
	v_add_u32_e32 v99, s9, v100
	s_waitcnt lgkmcnt(0)
	s_barrier
	ds_read_b128 v[34:37], v99 offset:0
	ds_read_b128 v[38:41], v99 offset:8192
	ds_read_b128 v[42:45], v99 offset:16384
	ds_read_b128 v[46:49], v99 offset:24576
	ds_read_b128 v[50:53], v99 offset:32768
	ds_read_b128 v[54:57], v99 offset:40960
	ds_read_b128 v[58:61], v99 offset:49152
	ds_read_b128 v[62:65], v99 offset:57344
	s_lshl_b32 s8, s27, 3
	s_add_u32 s8, s8, s23
	s_lshl_b32 s8, s8, 11
	s_lshl_b32 s9, s30, 10
	s_add_u32 s8, s8, s9
	s_add_u32 s28, s28, s8
	s_addc_u32 s29, s29, 0
	s_waitcnt lgkmcnt(6)
	v_pk_add_f32 v[34:35], v[34:35], v[38:39]
	v_pk_add_f32 v[36:37], v[36:37], v[40:41]
	s_waitcnt lgkmcnt(5)
	v_pk_add_f32 v[34:35], v[34:35], v[42:43]
	v_pk_add_f32 v[36:37], v[36:37], v[44:45]
	s_waitcnt lgkmcnt(4)
	v_pk_add_f32 v[34:35], v[34:35], v[46:47]
	v_pk_add_f32 v[36:37], v[36:37], v[48:49]
	s_waitcnt lgkmcnt(3)
	v_pk_add_f32 v[34:35], v[34:35], v[50:51]
	v_pk_add_f32 v[36:37], v[36:37], v[52:53]
	s_waitcnt lgkmcnt(2)
	v_pk_add_f32 v[34:35], v[34:35], v[54:55]
	v_pk_add_f32 v[36:37], v[36:37], v[56:57]
	s_waitcnt lgkmcnt(1)
	v_pk_add_f32 v[34:35], v[34:35], v[58:59]
	v_pk_add_f32 v[36:37], v[36:37], v[60:61]
	s_waitcnt lgkmcnt(0)
	v_pk_add_f32 v[34:35], v[34:35], v[62:63]
	v_pk_add_f32 v[36:37], v[36:37], v[64:65]
	global_store_dwordx4 v100, v[34:37], s[28:29]
